# speedup vs baseline: 1.0031x; 1.0018x over previous
.LBB4_35:
	s_or_b64 exec, exec, s[16:17]
	s_waitcnt vmcnt(0)
	ds_write_b128 v72, v[18:21] offset:52224
	v_and_b32_e32 v19, 16, v0
	v_add_u32_e32 v20, 14, v0
	s_load_dwordx2 s[6:7], s[0:1], 0x40
	v_and_b32_e32 v20, 15, v20
	v_cmp_eq_u32_e64 s[0:1], 0, v19
	v_or_b32_e32 v18, v105, v73
	v_mad_u32_u24 v80, v101, 6, 4
	v_cndmask_b32_e64 v19, v20, v98, s[0:1]
	v_mad_u32_u24 v21, v18, 18, v19
	v_lshl_or_b32 v18, v18, 4, v19
	s_movk_i32 s0, 0x50
	v_mov_b32_e32 v19, 0xfc00
	v_mad_u32_u24 v78, v18, s0, v19
	v_or_b32_e32 v18, v106, v98
	v_mul_u32_u24_e32 v22, 6, v101
	v_or_b32_e32 v81, 0xffffff60, v98
	v_mad_u32_u24 v18, v18, s0, v19
	s_movk_i32 s0, 0x60
	v_lshlrev_b32_e32 v95, 11, v80
	v_lshlrev_b32_e32 v80, 4, v80
	v_add_u32_e32 v83, 19, v98
	v_mul_u32_u24_e32 v24, 0x60, v101
	v_mad_u32_u24 v25, v101, s0, v81
	v_mov_b32_e32 v27, 0xffffff5d
	s_movk_i32 s0, 0x6c
	v_or_b32_e32 v22, 1, v22
	v_add_u32_e32 v90, v80, v81
	v_or_b32_e32 v91, v80, v98
	v_mad_u32_u24 v80, v101, 6, 5
	v_or_b32_e32 v24, v24, v98
	v_mad_i32_i24 v28, v25, 18, v27
	v_mad_u32_u24 v29, v101, s0, v83
	v_lshlrev_b32_e32 v31, 4, v22
	v_lshlrev_b32_e32 v97, 11, v80
	v_lshlrev_b32_e32 v80, 4, v80
	v_cmp_gt_u32_e64 s[0:1], 20, v25
	v_or_b32_e32 v23, v104, v98
	v_mul_i32_i24_e32 v26, 18, v25
	v_add_u32_e32 v32, v31, v81
	v_add_u32_e32 v104, v80, v81
	v_or_b32_e32 v105, v80, v98
	v_mul_u32_u24_e32 v80, 0x90, v21
	v_cndmask_b32_e64 v21, v24, v28, s[0:1]
	v_cmp_gt_i32_e64 s[0:1], 10, v25
	v_or_b32_e32 v31, v31, v98
	v_mad_i32_i24 v34, v32, 18, v27
	v_mad_u32_u24 v35, v101, 6, 2
	v_cndmask_b32_e64 v21, v21, v26, s[0:1]
	v_cmp_gt_u32_e64 s[0:1], 20, v32
	v_mul_i32_i24_e32 v33, 18, v32
	v_lshlrev_b32_e32 v36, 11, v35
	v_lshlrev_b32_e32 v35, 4, v35
	v_cndmask_b32_e64 v24, v31, v34, s[0:1]
	v_cmp_gt_i32_e64 s[0:1], 10, v32
	v_readfirstlane_b32 s10, v99
	v_lshlrev_b32_e32 v30, 11, v22
	v_mad_u32_u24 v22, v22, 18, v83
	v_add_u32_e32 v37, v35, v81
	v_mad_u32_u24 v77, v101, 6, 3
	v_cndmask_b32_e64 v24, v24, v33, s[0:1]
	s_mul_i32 s8, s10, 9
	s_lshl_b32 s25, s10, 4
	v_or_b32_e32 v35, v35, v98
	v_mad_i32_i24 v73, v37, 18, v27
	v_add_u32_e32 v76, 18, v22
	v_lshlrev_b32_e32 v93, 11, v77
	v_lshlrev_b32_e32 v77, 4, v77
	v_add_u32_e32 v89, 36, v22
	v_add_u32_e32 v96, 54, v22
	v_add_u32_e32 v107, 0x48, v22
	s_movk_i32 s10, 0x90
	v_cndmask_b32_e32 v21, v21, v29, vcc
	v_cndmask_b32_e32 v22, v24, v22, vcc
	v_cmp_gt_u32_e32 vcc, 20, v37
	v_add_u32_e32 v39, 0xcc00, v72
	v_mul_i32_i24_e32 v72, 18, v37
	v_add_u32_e32 v85, v77, v81
	v_mul_lo_u32 v24, v22, s10
	v_cndmask_b32_e32 v22, v35, v73, vcc
	v_cmp_gt_i32_e32 vcc, 10, v37
	v_or_b32_e32 v77, v77, v98
	v_mad_i32_i24 v88, v85, 18, v27
	v_cndmask_b32_e32 v22, v22, v72, vcc
	v_cmp_gt_u32_e32 vcc, 20, v85
	v_mul_i32_i24_e32 v87, 18, v85
	v_mad_i32_i24 v94, v90, 18, v27
	v_cndmask_b32_e32 v25, v77, v88, vcc
	v_cmp_gt_i32_e32 vcc, 10, v85
	v_mul_i32_i24_e32 v92, 18, v90
	v_mad_i32_i24 v27, v104, 18, v27
	v_cndmask_b32_e32 v25, v25, v87, vcc
	v_cmp_gt_u32_e32 vcc, 20, v90
	v_mul_i32_i24_e32 v106, 18, v104
	v_add_u32_e32 v82, 1, v98
	v_cndmask_b32_e32 v26, v91, v94, vcc
	v_cmp_gt_i32_e32 vcc, 10, v90
	v_add_u32_e32 v79, 0xa3, v98
	v_lshrrev_b32_e32 v85, 7, v0
	v_cndmask_b32_e32 v26, v26, v92, vcc
	v_cmp_gt_u32_e32 vcc, 20, v104
	s_movk_i32 s0, 0x70
	v_mul_u32_u24_e32 v38, 0xc0, v23
	v_cndmask_b32_e32 v27, v105, v27, vcc
	v_cmp_gt_i32_e32 vcc, 10, v104
	v_mov_b32_e32 v23, 0
	s_waitcnt lgkmcnt(0)
	s_barrier
	v_cndmask_b32_e64 v26, v26, v96, s[4:5]
	v_cndmask_b32_e32 v27, v27, v106, vcc
	v_cmp_ne_u32_e32 vcc, 0, v101
	v_cndmask_b32_e64 v27, v27, v107, s[4:5]
	s_ashr_i32 s9, s8, 31
	v_cndmask_b32_e32 v22, v22, v82, vcc
	v_cndmask_b32_e64 v22, v22, v76, s[4:5]
	v_mul_lo_u32 v28, v22, s10
	v_cndmask_b32_e32 v22, v25, v79, vcc
	v_cndmask_b32_e64 v22, v22, v89, s[4:5]
	v_mul_lo_u32 v25, v22, s10
	v_lshlrev_b32_e32 v22, 7, v98
	v_lshl_or_b32 v22, v85, 11, v22
	v_and_or_b32 v22, v0, s0, v22
	s_mov_b64 s[0:1], 0xc900
	v_or_b32_e32 v75, 0xcc00, v102
	v_or_b32_e32 v84, 0x6c00, v102
	v_lshl_or_b32 v20, v99, 5, v103
	v_mul_u32_u24_e32 v19, 0x3000, v101
	v_mul_lo_u32 v21, v21, s10
	v_mul_lo_u32 v26, v26, s10
	v_mul_lo_u32 v27, v27, s10
	v_lshl_add_u64 v[72:73], v[22:23], 0, s[0:1]
	v_lshl_or_b32 v22, v38, 1, v74
	s_mov_b64 s[0:1], 0x18400
	v_lshl_add_u32 v86, v99, 11, v75
	s_mov_b32 s23, 5
	v_lshl_add_u64 v[76:77], v[22:23], 0, s[0:1]
	s_lshl_b64 s[0:1], s[8:9], 4
	s_add_u32 s16, s20, s0
	s_addc_u32 s17, s21, s1
	s_load_dwordx8 s[36:43], s[16:17], 0x16900
	s_load_dwordx8 s[44:51], s[16:17], 0x16920
	s_load_dwordx8 s[52:59], s[16:17], 0x16940
	s_load_dwordx8 s[60:67], s[16:17], 0x16960
	s_load_dwordx4 s[68:71], s[16:17], 0x16980
	s_load_dwordx8 s[72:79], s[16:17], 0x16b40
	s_load_dwordx8 s[80:87], s[16:17], 0x16b60
	s_load_dwordx8 s[88:95], s[16:17], 0x16b80
	s_load_dwordx4 s[96:99], s[16:17], 0x16ba0
	s_load_dwordx8 s[8:15], s[16:17], 0x16bb0
	v_add_u32_e32 v87, v84, v19
	v_add_u32_e32 v88, v20, v21
	v_add_u32_e32 v89, v84, v30
	v_add_u32_e32 v90, v20, v24
	v_add_u32_e32 v91, v84, v36
	v_add_u32_e32 v92, v20, v28
	v_add_u32_e32 v93, v84, v93
	v_add_u32_e32 v94, v20, v25
	v_add_u32_e32 v95, v84, v95
	v_add_u32_e32 v96, v20, v26
	v_add_u32_e32 v97, v84, v97
	v_add_u32_e32 v101, v20, v27
	s_mov_b32 s31, 0x3e6d3387
	s_mov_b32 s22, 0xbf3a00e3
	s_mov_b32 s24, 0x3f07dc22
	s_mov_b32 s26, 0x3f35f0e3
	s_mov_b32 s28, 0xbe11a98e
	s_mov_b32 s30, 0x3e027906
	s_mov_b64 s[34:35], 0x2000
	v_mov_b32_e32 v104, 1.0
	v_add_u32_e32 v74, v18, v74
	v_readfirstlane_b32 s100, v85
	s_cmp_eq_u32 s100, 3
	s_cbranch_scc1 .Lp1_nt3
	s_mul_i32 s101, s100, 54
	s_add_i32 s101, s101, 19
	v_add_u32_e32 v88, s101, v98
	v_add_u32_e32 v90, 18, v88
	v_add_u32_e32 v92, 36, v88
	s_cmp_eq_u32 s100, 2
	s_cbranch_scc0 .Lp1_smap_done
	v_add_u32_e32 v92, 1, v98
	s_branch .Lp1_smap_done
.Lp1_nt3:
	v_add_u32_e32 v88, 0xa3, v98
	v_mul_u32_u24_e32 v90, 18, v98
	v_cmp_gt_u32_e64 s[100:101], 10, v98
	v_add_u32_e32 v92, 0xffffff5d, v90
	s_nop 0
	v_cndmask_b32_e64 v94, v92, v90, s[100:101]
	v_cmp_gt_u32_e64 s[100:101], 4, v98
	v_add_u32_e32 v96, 0x7d, v90
	v_add_u32_e32 v92, 0xb0, v98
	s_nop 0
	v_cndmask_b32_e64 v92, v92, v96, s[100:101]
	v_mov_b32_e32 v90, v94
.Lp1_smap_done:
	v_and_b32_e32 v94, 1, v99
	v_lshl_or_b32 v96, v94, 6, v103
	s_movk_i32 s100, 0x90
	v_mad_u32_u24 v88, v88, s100, v96
	v_mad_u32_u24 v90, v90, s100, v96
	v_mad_u32_u24 v92, v92, s100, v96
	v_lshl_add_u32 v86, v94, 12, v75
	s_movk_i32 s100, 0x1800
	v_mad_u32_u24 v96, v85, s100, v84
	ds_read_b128 v[40:43], v96
	ds_read_b128 v[44:47], v96 offset:1024
	ds_read_b128 v[48:51], v96 offset:2048
	ds_read_b128 v[52:55], v96 offset:3072
	ds_read_b128 v[56:59], v96 offset:4096
	ds_read_b128 v[60:63], v96 offset:5120
	s_lshr_b32 s101, s18, 8
	s_waitcnt lgkmcnt(0)
	s_branch .LBB4_37
.LBB4_36:
	s_or_b64 exec, exec, s[32:33]
	s_waitcnt lgkmcnt(0)
	s_barrier
	ds_read_b128 v[18:21], v75 offset:8192
	ds_read_b128 v[22:25], v74
	ds_read_b128 v[26:29], v75 offset:9216
	s_add_i32 s23, s23, -1
	s_add_u32 s0, s0, 0x480
	s_addc_u32 s1, s1, 0
	s_waitcnt lgkmcnt(1)
	v_mfma_f32_16x16x32_f16 v[2:5], v[18:21], v[22:25], v[2:5]
	ds_read_b128 v[18:21], v75 offset:10240
	v_lshl_add_u64 v[72:73], v[72:73], 0, s[34:35]
	s_cmp_eq_u32 s23, 0
	s_waitcnt lgkmcnt(1)
	v_mfma_f32_16x16x32_f16 v[6:9], v[26:29], v[22:25], v[6:9]
	ds_read_b128 v[26:29], v75 offset:11264
	v_lshl_add_u64 v[76:77], v[76:77], 0, 64
	s_waitcnt lgkmcnt(1)
	v_mfma_f32_16x16x32_f16 v[10:13], v[18:21], v[22:25], v[10:13]
	s_waitcnt lgkmcnt(0)
	v_mfma_f32_16x16x32_f16 v[14:17], v[26:29], v[22:25], v[14:17]
	s_cbranch_scc1 .LBB4_41
.LBB4_37:
	v_lshl_add_u64 v[18:19], s[20:21], 0, v[72:73]
	global_load_dwordx4 v[22:25], v[18:19], off
	v_mov_b32_e32 v18, 0
	v_mov_b32_e32 v19, 0
	v_mov_b32_e32 v20, 0
	v_mov_b32_e32 v21, 0
	s_and_saveexec_b64 s[32:33], s[4:5]
	s_cbranch_execz .LBB4_39
	v_lshl_add_u64 v[18:19], s[20:21], 0, v[76:77]
	global_load_dwordx4 v[18:21], v[18:19], off
.LBB4_39:
	s_or_b64 exec, exec, s[32:33]
	s_setprio 1
	ds_read_b128 v[26:29], v86
	ds_read_b128 v[30:33], v86 offset:1024
	ds_read_b128 v[106:109], v86 offset:2048
	ds_read_b128 v[110:113], v86 offset:3072
	s_waitcnt lgkmcnt(2)
	v_mfma_f32_16x16x32_f16 v[34:37], v[26:29], v[40:43], 0
	v_mfma_f32_16x16x32_f16 v[114:117], v[26:29], v[48:51], 0
	v_mfma_f32_16x16x32_f16 v[118:121], v[26:29], v[56:59], 0
	v_mfma_f32_16x16x32_f16 v[34:37], v[30:33], v[44:47], v[34:37]
	v_mfma_f32_16x16x32_f16 v[114:117], v[30:33], v[52:55], v[114:117]
	v_mfma_f32_16x16x32_f16 v[118:121], v[30:33], v[60:63], v[118:121]
	s_waitcnt lgkmcnt(0)
	v_mfma_f32_16x16x32_f16 v[122:125], v[106:109], v[40:43], 0
	v_mfma_f32_16x16x32_f16 v[122:125], v[110:113], v[44:47], v[122:125]
	s_nop 2
	v_cvt_pk_f16_f32 v34, v34, v35
	v_cvt_pk_f16_f32 v35, v36, v37
	ds_write_b64 v88, v[34:35]
	v_cvt_pk_f16_f32 v114, v114, v115
	v_cvt_pk_f16_f32 v115, v116, v117
	ds_write_b64 v90, v[114:115]
	v_cvt_pk_f16_f32 v118, v118, v119
	v_cvt_pk_f16_f32 v119, v120, v121
	ds_write_b64 v92, v[118:119]
	v_mfma_f32_16x16x32_f16 v[34:37], v[106:109], v[48:51], 0
	v_mfma_f32_16x16x32_f16 v[114:117], v[106:109], v[56:59], 0
	v_mfma_f32_16x16x32_f16 v[34:37], v[110:113], v[52:55], v[34:37]
	v_mfma_f32_16x16x32_f16 v[114:117], v[110:113], v[60:63], v[114:117]
	v_cvt_pk_f16_f32 v122, v122, v123
	v_cvt_pk_f16_f32 v123, v124, v125
	ds_write_b64 v88, v[122:123] offset:32
	s_nop 3
	v_cvt_pk_f16_f32 v34, v34, v35
	v_cvt_pk_f16_f32 v35, v36, v37
	ds_write_b64 v90, v[34:35] offset:32
	v_cvt_pk_f16_f32 v114, v114, v115
	v_cvt_pk_f16_f32 v115, v116, v117
	ds_write_b64 v92, v[114:115] offset:32
	s_setprio 0
	s_waitcnt lgkmcnt(0)
	s_barrier
	v_add_u32_e32 v105, s25, v80
	ds_read_b128 v[30:33], v105
	ds_read_b128 v[34:37], v105 offset:64
	ds_read_b128 v[106:109], v105 offset:144
	ds_read_b128 v[110:113], v105 offset:208
	ds_read_b128 v[114:117], v105 offset:288
	ds_read_b128 v[122:125], v105 offset:352
	s_waitcnt lgkmcnt(4)
	v_pk_fma_f16 v118, v30, s36, 0
	v_pk_fma_f16 v119, v31, s37, 0
	v_pk_fma_f16 v120, v32, s38, 0
	v_pk_fma_f16 v121, v33, s39, 0
	v_pk_fma_f16 v26, v34, s72, 0
	v_pk_fma_f16 v27, v35, s73, 0
	v_pk_fma_f16 v28, v36, s74, 0
	v_pk_fma_f16 v29, v37, s75, 0
	ds_read_b128 v[30:33], v105 offset:2592
	ds_read_b128 v[34:37], v105 offset:2656
	s_waitcnt lgkmcnt(4)
	v_pk_fma_f16 v118, v106, s40, v118
	v_pk_fma_f16 v119, v107, s41, v119
	v_pk_fma_f16 v120, v108, s42, v120
	v_pk_fma_f16 v121, v109, s43, v121
	v_pk_fma_f16 v26, v110, s76, v26
	v_pk_fma_f16 v27, v111, s77, v27
	v_pk_fma_f16 v28, v112, s78, v28
	v_pk_fma_f16 v29, v113, s79, v29
	ds_read_b128 v[106:109], v105 offset:2736
	ds_read_b128 v[110:113], v105 offset:2800
	s_waitcnt lgkmcnt(4)
	v_pk_fma_f16 v118, v114, s44, v118
	v_pk_fma_f16 v119, v115, s45, v119
	v_pk_fma_f16 v120, v116, s46, v120
	v_pk_fma_f16 v121, v117, s47, v121
	v_pk_fma_f16 v26, v122, s80, v26
	v_pk_fma_f16 v27, v123, s81, v27
	v_pk_fma_f16 v28, v124, s82, v28
	v_pk_fma_f16 v29, v125, s83, v29
	ds_read_b128 v[114:117], v105 offset:2880
	ds_read_b128 v[122:125], v105 offset:2944
	s_waitcnt lgkmcnt(4)
	v_pk_fma_f16 v118, v30, s48, v118
	v_pk_fma_f16 v119, v31, s49, v119
	v_pk_fma_f16 v120, v32, s50, v120
	v_pk_fma_f16 v121, v33, s51, v121
	v_pk_fma_f16 v26, v34, s84, v26
	v_pk_fma_f16 v27, v35, s85, v27
	v_pk_fma_f16 v28, v36, s86, v28
	v_pk_fma_f16 v29, v37, s87, v29
	ds_read_b128 v[30:33], v105 offset:5184
	ds_read_b128 v[34:37], v105 offset:5248
	s_waitcnt lgkmcnt(4)
	v_pk_fma_f16 v118, v106, s52, v118
	v_pk_fma_f16 v119, v107, s53, v119
	v_pk_fma_f16 v120, v108, s54, v120
	v_pk_fma_f16 v121, v109, s55, v121
	v_pk_fma_f16 v26, v110, s88, v26
	v_pk_fma_f16 v27, v111, s89, v27
	v_pk_fma_f16 v28, v112, s90, v28
	v_pk_fma_f16 v29, v113, s91, v29
	ds_read_b128 v[106:109], v105 offset:5328
	ds_read_b128 v[110:113], v105 offset:5392
	s_waitcnt lgkmcnt(4)
	v_pk_fma_f16 v118, v114, s56, v118
	v_pk_fma_f16 v119, v115, s57, v119
	v_pk_fma_f16 v120, v116, s58, v120
	v_pk_fma_f16 v121, v117, s59, v121
	v_pk_fma_f16 v26, v122, s92, v26
	v_pk_fma_f16 v27, v123, s93, v27
	v_pk_fma_f16 v28, v124, s94, v28
	v_pk_fma_f16 v29, v125, s95, v29
	ds_read_b128 v[114:117], v105 offset:5472
	ds_read_b128 v[122:125], v105 offset:5536
	s_waitcnt lgkmcnt(4)
	v_pk_fma_f16 v118, v30, s60, v118
	v_pk_fma_f16 v119, v31, s61, v119
	v_pk_fma_f16 v120, v32, s62, v120
	v_pk_fma_f16 v121, v33, s63, v121
	v_pk_fma_f16 v26, v34, s96, v26
	v_pk_fma_f16 v27, v35, s97, v27
	v_pk_fma_f16 v28, v36, s98, v28
	v_pk_fma_f16 v29, v37, s99, v29
	s_waitcnt lgkmcnt(2)
	v_pk_fma_f16 v118, v106, s64, v118
	v_pk_fma_f16 v119, v107, s65, v119
	v_pk_fma_f16 v120, v108, s66, v120
	v_pk_fma_f16 v121, v109, s67, v121
	v_pk_fma_f16 v26, v110, s8, v26
	v_pk_fma_f16 v27, v111, s9, v27
	v_pk_fma_f16 v28, v112, s10, v28
	v_pk_fma_f16 v29, v113, s11, v29
	s_waitcnt lgkmcnt(0)
	v_pk_fma_f16 v26, v122, s12, v26
	v_pk_fma_f16 v27, v123, s13, v27
	v_pk_fma_f16 v28, v124, s14, v28
	v_pk_fma_f16 v29, v125, s15, v29
	v_pk_fma_f16 v109, v114, s68, v118
	v_pk_fma_f16 v123, v115, s69, v119
	v_pk_fma_f16 v122, v116, s70, v120
	v_pk_fma_f16 v105, v117, s71, v121
	s_add_u32 s16, s20, s0
	s_addc_u32 s17, s21, s1
	s_load_dwordx8 s[36:43], s[16:17], 0x16d80
	s_load_dwordx8 s[44:51], s[16:17], 0x16da0
	s_load_dwordx8 s[52:59], s[16:17], 0x16dc0
	s_load_dwordx8 s[60:67], s[16:17], 0x16de0
	s_load_dwordx4 s[68:71], s[16:17], 0x16e00
	s_load_dwordx8 s[72:79], s[16:17], 0x16fc0
	s_load_dwordx8 s[80:87], s[16:17], 0x16fe0
	s_load_dwordx8 s[88:95], s[16:17], 0x17000
	s_load_dwordx4 s[96:99], s[16:17], 0x17020
	s_load_dwordx8 s[8:15], s[16:17], 0x17030
	v_mov_b64_e32 v[114:115], s[22:23]
	v_cvt_f32_f16_e32 v112, v109
	v_cvt_f32_f16_sdwa v113, v109 dst_sel:DWORD dst_unused:UNUSED_PAD src0_sel:WORD_1
	v_fma_mix_f32 v108, |v109|, s31, v104 op_sel_hi:[1,0,0]
	v_fma_mix_f32 v109, |v109|, s31, v104 op_sel:[1,0,0] op_sel_hi:[1,0,0]
	v_rcp_f32_e32 v108, v108
	v_rcp_f32_e32 v109, v109
	v_mul_f32_e32 v110, 0x3f596d27, v112
	v_mul_f32_e32 v111, 0x3f596d27, v113
	v_mul_f32_e64 v110, v110, -v110
	v_pk_fma_f32 v[116:117], v[108:109], s[24:25], v[114:115] op_sel_hi:[1,0,0]
	v_mul_f32_e64 v111, v111, -v111
	v_exp_f32_e32 v110, v110
	v_pk_fma_f32 v[116:117], v[116:117], v[108:109], s[26:27] op_sel_hi:[1,1,0]
	v_exp_f32_e32 v111, v111
	v_pk_fma_f32 v[116:117], v[116:117], v[108:109], s[28:29] op_sel_hi:[1,1,0]
	v_and_b32_e32 v106, 0x7fffffff, v112
	v_pk_fma_f32 v[116:117], v[116:117], v[108:109], s[30:31] op_sel_hi:[1,1,0]
	v_and_b32_e32 v107, 0x7fffffff, v113
	v_pk_mul_f32 v[108:109], v[108:109], v[116:117]
	v_max_f32_e32 v112, 0, v112
	v_pk_mul_f32 v[108:109], v[110:111], v[108:109]
	v_max_f32_e32 v113, 0, v113
	v_cvt_f32_f16_e32 v111, v123
	v_cvt_f32_f16_sdwa v124, v123 dst_sel:DWORD dst_unused:UNUSED_PAD src0_sel:WORD_1
	v_pk_fma_f32 v[106:107], v[106:107], v[108:109], v[112:113] neg_lo:[1,0,0] neg_hi:[1,0,0]
	v_fma_mix_f32 v108, |v123|, s31, v104 op_sel_hi:[1,0,0]
	v_fma_mix_f32 v109, |v123|, s31, v104 op_sel:[1,0,0] op_sel_hi:[1,0,0]
	v_rcp_f32_e32 v108, v108
	v_rcp_f32_e32 v109, v109
	v_cvt_pk_f16_f32 v125, v106, v107
	v_and_b32_e32 v106, 0x7fffffff, v111
	v_mul_f32_e32 v110, 0x3f596d27, v111
	v_max_f32_e32 v112, 0, v111
	v_mul_f32_e32 v111, 0x3f596d27, v124
	v_mul_f32_e64 v110, v110, -v110
	v_pk_fma_f32 v[116:117], v[108:109], s[24:25], v[114:115] op_sel_hi:[1,0,0]
	v_mul_f32_e64 v111, v111, -v111
	v_exp_f32_e32 v110, v110
	v_pk_fma_f32 v[116:117], v[116:117], v[108:109], s[26:27] op_sel_hi:[1,1,0]
	v_exp_f32_e32 v111, v111
	v_pk_fma_f32 v[116:117], v[116:117], v[108:109], s[28:29] op_sel_hi:[1,1,0]
	v_and_b32_e32 v107, 0x7fffffff, v124
	v_pk_fma_f32 v[116:117], v[116:117], v[108:109], s[30:31] op_sel_hi:[1,1,0]
	v_max_f32_e32 v113, 0, v124
	v_pk_mul_f32 v[108:109], v[108:109], v[116:117]
	v_cvt_f32_f16_sdwa v123, v122 dst_sel:DWORD dst_unused:UNUSED_PAD src0_sel:WORD_1
	v_pk_mul_f32 v[108:109], v[110:111], v[108:109]
	v_cvt_f32_f16_e32 v111, v122
	v_pk_fma_f32 v[106:107], v[106:107], v[108:109], v[112:113] neg_lo:[1,0,0] neg_hi:[1,0,0]
	v_fma_mix_f32 v108, |v122|, s31, v104 op_sel_hi:[1,0,0]
	v_fma_mix_f32 v109, |v122|, s31, v104 op_sel:[1,0,0] op_sel_hi:[1,0,0]
	v_rcp_f32_e32 v108, v108
	v_rcp_f32_e32 v109, v109
	v_cvt_pk_f16_f32 v124, v106, v107
	v_and_b32_e32 v106, 0x7fffffff, v111
	v_mul_f32_e32 v110, 0x3f596d27, v111
	v_max_f32_e32 v112, 0, v111
	v_mul_f32_e32 v111, 0x3f596d27, v123
	v_mul_f32_e64 v110, v110, -v110
	v_pk_fma_f32 v[116:117], v[108:109], s[24:25], v[114:115] op_sel_hi:[1,0,0]
	v_mul_f32_e64 v111, v111, -v111
	v_exp_f32_e32 v110, v110
	v_pk_fma_f32 v[116:117], v[116:117], v[108:109], s[26:27] op_sel_hi:[1,1,0]
	v_exp_f32_e32 v111, v111
	v_pk_fma_f32 v[116:117], v[116:117], v[108:109], s[28:29] op_sel_hi:[1,1,0]
	v_and_b32_e32 v107, 0x7fffffff, v123
	v_pk_fma_f32 v[116:117], v[116:117], v[108:109], s[30:31] op_sel_hi:[1,1,0]
	v_max_f32_e32 v113, 0, v123
	v_pk_mul_f32 v[108:109], v[108:109], v[116:117]
	v_cvt_f32_f16_sdwa v116, v105 dst_sel:DWORD dst_unused:UNUSED_PAD src0_sel:WORD_1
	v_pk_mul_f32 v[108:109], v[110:111], v[108:109]
	v_cvt_f32_f16_e32 v111, v105
	v_pk_fma_f32 v[106:107], v[106:107], v[108:109], v[112:113] neg_lo:[1,0,0] neg_hi:[1,0,0]
	v_fma_mix_f32 v108, |v105|, s31, v104 op_sel_hi:[1,0,0]
	v_fma_mix_f32 v105, |v105|, s31, v104 op_sel:[1,0,0] op_sel_hi:[1,0,0]
	v_rcp_f32_e32 v108, v108
	v_rcp_f32_e32 v109, v105
	v_mul_f32_e32 v110, 0x3f596d27, v111
	v_mul_f32_e64 v105, v110, -v110
	v_exp_f32_e32 v110, v105
	v_mul_f32_e32 v105, 0x3f596d27, v116
	v_pk_fma_f32 v[114:115], v[108:109], s[24:25], v[114:115] op_sel_hi:[1,0,0]
	v_mul_f32_e64 v105, v105, -v105
	v_cvt_pk_f16_f32 v117, v106, v107
	v_and_b32_e32 v106, 0x7fffffff, v111
	v_max_f32_e32 v112, 0, v111
	v_pk_fma_f32 v[114:115], v[114:115], v[108:109], s[26:27] op_sel_hi:[1,1,0]
	v_exp_f32_e32 v111, v105
	v_pk_fma_f32 v[114:115], v[114:115], v[108:109], s[28:29] op_sel_hi:[1,1,0]
	v_and_b32_e32 v107, 0x7fffffff, v116
	v_pk_fma_f32 v[114:115], v[114:115], v[108:109], s[30:31] op_sel_hi:[1,1,0]
	v_max_f32_e32 v113, 0, v116
	v_pk_mul_f32 v[108:109], v[108:109], v[114:115]
	v_pk_mul_f32 v[108:109], v[110:111], v[108:109]
	v_pk_fma_f32 v[106:107], v[106:107], v[108:109], v[112:113] neg_lo:[1,0,0] neg_hi:[1,0,0]
	v_cvt_pk_f16_f32 v105, v106, v107
	v_pk_mul_f16 v28, v28, v117
	v_pk_mul_f16 v29, v29, v105
	v_pk_mul_f16 v27, v27, v124
	v_pk_mul_f16 v26, v26, v125
	v_add_u32_e32 v30, s25, v78
	ds_write_b128 v30, v[26:29]
	s_waitcnt vmcnt(0)
	ds_write_b128 v39, v[22:25]
	s_and_saveexec_b64 s[32:33], s[4:5]
	s_cbranch_execz .LBB4_36
	ds_write_b128 v39, v[18:21] offset:8192
	s_branch .LBB4_36
.LBB4_41:
	v_mbcnt_lo_u32_b32 v126, -1, 0
	v_mbcnt_hi_u32_b32 v126, -1, v126
	v_bfe_u32 v126, v126, 4, 2
	v_lshl_or_b32 v126, v126, 2, s101
	v_or_b32_e32 v40, 0, v126
	v_lshlrev_b32_e32 v40, 16, v40
	v_mov_b32_e32 v41, 0
	v_or_b32_e32 v42, 1, v126
	v_lshlrev_b32_e32 v42, 16, v42
	v_mov_b32_e32 v43, 0
	v_or_b32_e32 v44, 2, v126
	v_lshlrev_b32_e32 v44, 16, v44
	v_mov_b32_e32 v45, 0
	v_or_b32_e32 v46, 3, v126
	v_lshlrev_b32_e32 v46, 16, v46
	v_mov_b32_e32 v47, 0
	v_or_b32_e32 v48, 16, v126
	v_lshlrev_b32_e32 v48, 16, v48
	v_mov_b32_e32 v49, 0
	v_or_b32_e32 v50, 17, v126
	v_lshlrev_b32_e32 v50, 16, v50
	v_mov_b32_e32 v51, 0
	v_or_b32_e32 v52, 18, v126
	v_lshlrev_b32_e32 v52, 16, v52
	v_mov_b32_e32 v53, 0
	v_or_b32_e32 v54, 19, v126
	v_lshlrev_b32_e32 v54, 16, v54
	v_mov_b32_e32 v55, 0
	v_or_b32_e32 v56, 32, v126
	v_lshlrev_b32_e32 v56, 16, v56
	v_mov_b32_e32 v57, 0
	v_or_b32_e32 v58, 33, v126
	v_lshlrev_b32_e32 v58, 16, v58
	v_mov_b32_e32 v59, 0
	v_or_b32_e32 v60, 34, v126
	v_lshlrev_b32_e32 v60, 16, v60
	v_mov_b32_e32 v61, 0
	v_or_b32_e32 v62, 35, v126
	v_lshlrev_b32_e32 v62, 16, v62
	v_mov_b32_e32 v63, 0
	v_mov_b32_e32 v18, 0
	v_mov_b32_e32 v19, 0
	v_mov_b32_e32 v20, 0
	v_mov_b32_e32 v21, 0
	s_and_saveexec_b64 s[0:1], s[4:5]
	s_cbranch_execz .LBB4_43
	v_lshlrev_b32_e32 v18, 1, v38
	v_mov_b32_e32 v19, 0
	v_lshl_add_u64 v[20:21], s[20:21], 0, v[18:19]
	v_lshlrev_b32_e32 v18, 1, v103
	v_lshl_add_u64 v[18:19], v[20:21], 0, v[18:19]
	v_add_co_u32_e32 v18, vcc, 0x18000, v18
	s_nop 1
	v_addc_co_u32_e32 v19, vcc, 0, v19, vcc
	global_load_dwordx4 v[18:21], v[18:19], off offset:1344

	.amdhsa_kernel _Z8k4_fusedPKfPKDF16_S2_S0_S0_S2_S0_S0_Pf
		.amdhsa_group_segment_fixed_size 74752
		.amdhsa_private_segment_fixed_size 0
		.amdhsa_kernarg_size 72
		.amdhsa_user_sgpr_count 2
		.amdhsa_user_sgpr_dispatch_ptr 0
		.amdhsa_user_sgpr_queue_ptr 0
		.amdhsa_user_sgpr_kernarg_segment_ptr 1
		.amdhsa_user_sgpr_dispatch_id 0
		.amdhsa_user_sgpr_kernarg_preload_length 0
		.amdhsa_user_sgpr_kernarg_preload_offset 0
		.amdhsa_user_sgpr_private_segment_size 0
		.amdhsa_uses_dynamic_stack 0
		.amdhsa_enable_private_segment 0
		.amdhsa_system_sgpr_workgroup_id_x 1
		.amdhsa_system_sgpr_workgroup_id_y 0
		.amdhsa_system_sgpr_workgroup_id_z 0
		.amdhsa_system_sgpr_workgroup_info 0
		.amdhsa_system_vgpr_workitem_id 0
		.amdhsa_next_free_vgpr 128
		.amdhsa_next_free_sgpr 102
		.amdhsa_accum_offset 128
		.amdhsa_reserve_vcc 1
		.amdhsa_float_round_mode_32 0
		.amdhsa_float_round_mode_16_64 0
		.amdhsa_float_denorm_mode_32 3
		.amdhsa_float_denorm_mode_16_64 3
		.amdhsa_dx10_clamp 1
		.amdhsa_ieee_mode 1
		.amdhsa_fp16_overflow 0
		.amdhsa_tg_split 0
		.amdhsa_exception_fp_ieee_invalid_op 0
		.amdhsa_exception_fp_denorm_src 0
		.amdhsa_exception_fp_ieee_div_zero 0
		.amdhsa_exception_fp_ieee_overflow 0
		.amdhsa_exception_fp_ieee_underflow 0
		.amdhsa_exception_fp_ieee_inexact 0
		.amdhsa_exception_int_div_zero 0
	.end_amdhsa_kernel

amdhsa.kernels:
  - .agpr_count:     0
    .args:
      - .actual_access:  read_only
        .address_space:  global
        .offset:         0
        .size:           8
        .value_kind:     global_buffer
      - .actual_access:  read_only
        .address_space:  global
        .offset:         8
        .size:           8
        .value_kind:     global_buffer
      - .actual_access:  read_only
        .address_space:  global
        .offset:         16
        .size:           8
        .value_kind:     global_buffer
      - .actual_access:  read_only
        .address_space:  global
        .offset:         24
        .size:           8
        .value_kind:     global_buffer
      - .actual_access:  write_only
        .address_space:  global
        .offset:         32
        .size:           8
        .value_kind:     global_buffer
      - .actual_access:  write_only
        .address_space:  global
        .offset:         40
        .size:           8
        .value_kind:     global_buffer
      - .actual_access:  write_only
        .address_space:  global
        .offset:         48
        .size:           8
        .value_kind:     global_buffer
      - .actual_access:  read_only
        .address_space:  global
        .offset:         56
        .size:           8
        .value_kind:     global_buffer
      - .actual_access:  read_only
        .address_space:  global
        .offset:         64
        .size:           8
        .value_kind:     global_buffer
      - .actual_access:  read_only
        .address_space:  global
        .offset:         72
        .size:           8
        .value_kind:     global_buffer
      - .actual_access:  read_only
        .address_space:  global
        .offset:         80
        .size:           8
        .value_kind:     global_buffer
      - .actual_access:  read_only
        .address_space:  global
        .offset:         88
        .size:           8
        .value_kind:     global_buffer
      - .actual_access:  read_only
        .address_space:  global
        .offset:         96
        .size:           8
        .value_kind:     global_buffer
      - .actual_access:  read_only
        .address_space:  global
        .offset:         104
        .size:           8
        .value_kind:     global_buffer
      - .actual_access:  write_only
        .address_space:  global
        .offset:         112
        .size:           8
        .value_kind:     global_buffer
    .group_segment_fixed_size: 18176
    .kernarg_segment_align: 8
    .kernarg_segment_size: 120
    .language:       OpenCL C
    .language_version:
      - 2
      - 0
    .max_flat_workgroup_size: 256
    .name:           _Z5k0_lnPKfS0_S0_S0_PDF16_S1_S1_S0_S0_S0_S0_S0_S0_S0_S1_
    .private_segment_fixed_size: 0
    .sgpr_count:     31
    .sgpr_spill_count: 0
    .symbol:         _Z5k0_lnPKfS0_S0_S0_PDF16_S1_S1_S0_S0_S0_S0_S0_S0_S0_S1_.kd
    .uniform_work_group_size: 1
    .uses_dynamic_stack: false
    .vgpr_count:     67
    .vgpr_spill_count: 0
    .wavefront_size: 64
  - .agpr_count:     0
    .args:
      - .actual_access:  read_only
        .address_space:  global
        .offset:         0
        .size:           8
        .value_kind:     global_buffer
      - .actual_access:  read_only
        .address_space:  global
        .offset:         8
        .size:           8
        .value_kind:     global_buffer
      - .actual_access:  read_only
        .address_space:  global
        .offset:         16
        .size:           8
        .value_kind:     global_buffer
      - .actual_access:  read_only
        .address_space:  global
        .offset:         24
        .size:           8
        .value_kind:     global_buffer
      - .actual_access:  read_only
        .address_space:  global
        .offset:         32
        .size:           8
        .value_kind:     global_buffer
      - .actual_access:  write_only
        .address_space:  global
        .offset:         40
        .size:           8
        .value_kind:     global_buffer
    .group_segment_fixed_size: 149200
    .kernarg_segment_align: 8
    .kernarg_segment_size: 48
    .language:       OpenCL C
    .language_version:
      - 2
      - 0
    .max_flat_workgroup_size: 1024
    .name:           _Z6k1_mfePKDF16_PKfS2_S2_S2_PDF16_
    .private_segment_fixed_size: 0
    .sgpr_count:     30
    .sgpr_spill_count: 0
    .symbol:         _Z6k1_mfePKDF16_PKfS2_S2_S2_PDF16_.kd
    .uniform_work_group_size: 1
    .uses_dynamic_stack: false
    .vgpr_count:     50
    .vgpr_spill_count: 0
    .wavefront_size: 64
  - .agpr_count:     0
    .args:
      - .actual_access:  read_only
        .address_space:  global
        .offset:         0
        .size:           8
        .value_kind:     global_buffer
      - .actual_access:  read_only
        .address_space:  global
        .offset:         8
        .size:           8
        .value_kind:     global_buffer
      - .actual_access:  read_only
        .address_space:  global
        .offset:         16
        .size:           8
        .value_kind:     global_buffer
      - .actual_access:  read_only
        .address_space:  global
        .offset:         24
        .size:           8
        .value_kind:     global_buffer
      - .actual_access:  write_only
        .address_space:  global
        .offset:         32
        .size:           8
        .value_kind:     global_buffer
      - .actual_access:  write_only
        .address_space:  global
        .offset:         40
        .size:           8
        .value_kind:     global_buffer
      - .actual_access:  write_only
        .address_space:  global
        .offset:         48
        .size:           8
        .value_kind:     global_buffer
    .group_segment_fixed_size: 71424
    .kernarg_segment_align: 8
    .kernarg_segment_size: 56
    .language:       OpenCL C
    .language_version:
      - 2
      - 0
    .max_flat_workgroup_size: 512
    .name:           _Z5k2_kvPKDF16_S0_S0_S0_PDF16_S1_Pf
    .private_segment_fixed_size: 0
    .sgpr_count:     33
    .sgpr_spill_count: 0
    .symbol:         _Z5k2_kvPKDF16_S0_S0_S0_PDF16_S1_Pf.kd
    .uniform_work_group_size: 1
    .uses_dynamic_stack: false
    .vgpr_count:     114
    .vgpr_spill_count: 0
    .wavefront_size: 64
  - .agpr_count:     0
    .args:
      - .actual_access:  read_only
        .address_space:  global
        .offset:         0
        .size:           8
        .value_kind:     global_buffer
      - .actual_access:  write_only
        .address_space:  global
        .offset:         8
        .size:           8
        .value_kind:     global_buffer
    .group_segment_fixed_size: 1024
    .kernarg_segment_align: 8
    .kernarg_segment_size: 16
    .language:       OpenCL C
    .language_version:
      - 2
      - 0
    .max_flat_workgroup_size: 256
    .name:           _Z9k3_reducePKfPf
    .private_segment_fixed_size: 0
    .sgpr_count:     13
    .sgpr_spill_count: 0
    .symbol:         _Z9k3_reducePKfPf.kd
    .uniform_work_group_size: 1
    .uses_dynamic_stack: false
    .vgpr_count:     50
    .vgpr_spill_count: 0
    .wavefront_size: 64
  - .agpr_count:     0
    .args:
      - .actual_access:  read_only
        .address_space:  global
        .offset:         0
        .size:           8
        .value_kind:     global_buffer
      - .actual_access:  read_only
        .address_space:  global
        .offset:         8
        .size:           8
        .value_kind:     global_buffer
      - .actual_access:  read_only
        .address_space:  global
        .offset:         16
        .size:           8
        .value_kind:     global_buffer
      - .actual_access:  read_only
        .address_space:  global
        .offset:         24
        .size:           8
        .value_kind:     global_buffer
      - .actual_access:  read_only
        .address_space:  global
        .offset:         32
        .size:           8
        .value_kind:     global_buffer
      - .actual_access:  read_only
        .address_space:  global
        .offset:         40
        .size:           8
        .value_kind:     global_buffer
      - .actual_access:  read_only
        .address_space:  global
        .offset:         48
        .size:           8
        .value_kind:     global_buffer
      - .actual_access:  read_only
        .address_space:  global
        .offset:         56
        .size:           8
        .value_kind:     global_buffer
      - .actual_access:  write_only
        .address_space:  global
        .offset:         64
        .size:           8
        .value_kind:     global_buffer
    .group_segment_fixed_size: 74752
    .kernarg_segment_align: 8
    .kernarg_segment_size: 72
    .language:       OpenCL C
    .language_version:
      - 2
      - 0
    .max_flat_workgroup_size: 512
    .name:           _Z8k4_fusedPKfPKDF16_S2_S0_S0_S2_S0_S0_Pf
    .private_segment_fixed_size: 0
    .sgpr_count:     108
    .sgpr_spill_count: 0
    .symbol:         _Z8k4_fusedPKfPKDF16_S2_S0_S0_S2_S0_S0_Pf.kd
    .uniform_work_group_size: 1
    .uses_dynamic_stack: false
    .vgpr_count:     128
    .vgpr_spill_count: 0
    .wavefront_size: 64
